# weight-conversion ticket f32 loads (phase W + GEMM tails) marked nt (once-read stream), on top of prologue + chain DMA reorder
# baseline (speedup 1.0000x reference)
; #define GAS __attribute__((address_space(1)))
; DI void w_load(const WItem& w, int lane, float (&v)[32]) {
;     const int cc = lane & 31, ccl = cc < w.nv ? cc : 0; const GAS float* wp = (const GAS float*)w.W + (size_t)(64 * w.kb + (lane >> 5)) * w.N + w.c0 + ccl;
; #pragma unroll
;     for (int i = 0; i < 32; ++i) v[i] = wp[(size_t)(2 * i) * w.N];
; }
; DI void w_tickets(LAS unsigned char* lds, const Ctx& c, int l, int budget) {
;     ...
;         if (i0 < W_NITEMS) { wa = w_decode(c, l, i0); w_load(wa, lane, va); }
.LBB0_59:
	s_waitcnt vmcnt(0)
	v_lshl_or_b32 v6, s86, 6, v39
	v_cmp_gt_u32_e32 vcc, s87, v1
	v_mul_hi_u32_u24_e32 v7, s74, v6
	v_mul_u32_u24_e32 v6, s74, v6
	v_cndmask_b32_e32 v8, 0, v1, vcc
	v_lshl_add_u64 v[6:7], v[6:7], 2, s[60:61]
	s_ashr_i32 s43, s42, 31
	v_lshl_add_u64 v[6:7], s[42:43], 2, v[6:7]
	v_lshlrev_b32_e32 v8, 2, v8
	v_mov_b32_e32 v9, v4
	v_lshl_add_u64 v[6:7], v[6:7], 0, v[8:9]
	s_lshl_b32 s68, s74, 3
	v_lshl_add_u64 v[8:9], v[6:7], 0, s[68:69]
	v_lshl_add_u64 v[10:11], v[8:9], 0, s[68:69]
	v_lshl_add_u64 v[12:13], v[10:11], 0, s[68:69]
	v_lshl_add_u64 v[14:15], v[12:13], 0, s[68:69]
	v_lshl_add_u64 v[16:17], v[14:15], 0, s[68:69]
	v_lshl_add_u64 v[18:19], v[16:17], 0, s[68:69]
	global_load_dword v6, v[6:7], off nt
	s_nop 0
	global_load_dword v7, v[8:9], off nt
	s_nop 0
	global_load_dword v8, v[10:11], off nt
	global_load_dword v9, v[12:13], off nt
	s_nop 0
	global_load_dword v10, v[14:15], off nt
	global_load_dword v11, v[16:17], off nt
	global_load_dword v12, v[18:19], off nt
	v_lshl_add_u64 v[14:15], v[18:19], 0, s[68:69]
	v_lshl_add_u64 v[16:17], v[14:15], 0, s[68:69]
	global_load_dword v13, v[14:15], off nt
	s_nop 0
	global_load_dword v14, v[16:17], off nt
	v_lshl_add_u64 v[16:17], v[16:17], 0, s[68:69]
	v_lshl_add_u64 v[18:19], v[16:17], 0, s[68:69]
	global_load_dword v15, v[16:17], off nt
	s_nop 0
	global_load_dword v16, v[18:19], off nt
	v_lshl_add_u64 v[18:19], v[18:19], 0, s[68:69]
	v_lshl_add_u64 v[20:21], v[18:19], 0, s[68:69]
	global_load_dword v17, v[18:19], off nt
	s_nop 0
	global_load_dword v18, v[20:21], off nt
	v_lshl_add_u64 v[20:21], v[20:21], 0, s[68:69]
	v_lshl_add_u64 v[22:23], v[20:21], 0, s[68:69]
	global_load_dword v19, v[20:21], off nt
	s_nop 0
	global_load_dword v20, v[22:23], off nt
	v_lshl_add_u64 v[22:23], v[22:23], 0, s[68:69]
	v_lshl_add_u64 v[24:25], v[22:23], 0, s[68:69]
	global_load_dword v21, v[22:23], off nt
	s_nop 0
	global_load_dword v22, v[24:25], off nt
	v_lshl_add_u64 v[24:25], v[24:25], 0, s[68:69]
	v_lshl_add_u64 v[26:27], v[24:25], 0, s[68:69]
	global_load_dword v23, v[24:25], off nt
	s_nop 0
	global_load_dword v24, v[26:27], off nt
	v_lshl_add_u64 v[26:27], v[26:27], 0, s[68:69]
	v_lshl_add_u64 v[28:29], v[26:27], 0, s[68:69]
	global_load_dword v25, v[26:27], off nt
	s_nop 0
	global_load_dword v26, v[28:29], off nt
	v_lshl_add_u64 v[28:29], v[28:29], 0, s[68:69]
	v_lshl_add_u64 v[30:31], v[28:29], 0, s[68:69]
	global_load_dword v27, v[28:29], off nt
	s_nop 0
	global_load_dword v28, v[30:31], off nt
	v_lshl_add_u64 v[30:31], v[30:31], 0, s[68:69]
	v_lshl_add_u64 v[32:33], v[30:31], 0, s[68:69]
	global_load_dword v29, v[30:31], off nt
	s_nop 0
	global_load_dword v30, v[32:33], off nt
	v_lshl_add_u64 v[32:33], v[32:33], 0, s[68:69]
	v_lshl_add_u64 v[34:35], v[32:33], 0, s[68:69]
	global_load_dword v31, v[32:33], off nt
	s_nop 0
	global_load_dword v32, v[34:35], off nt
	v_lshl_add_u64 v[34:35], v[34:35], 0, s[68:69]
	v_lshl_add_u64 v[36:37], v[34:35], 0, s[68:69]
	global_load_dword v33, v[34:35], off nt
	s_nop 0
	global_load_dword v34, v[36:37], off nt
	v_lshl_add_u64 v[36:37], v[36:37], 0, s[68:69]
	v_lshl_add_u64 v[78:79], v[36:37], 0, s[68:69]
	global_load_dword v35, v[36:37], off nt
	s_nop 0
	global_load_dword v36, v[78:79], off nt
	v_lshl_add_u64 v[78:79], v[78:79], 0, s[68:69]
	global_load_dword v37, v[78:79], off nt

; #define GAS __attribute__((address_space(1)))
; DI void w_load(const WItem& w, int lane, float (&v)[32]) {
;     const int cc = lane & 31, ccl = cc < w.nv ? cc : 0; const GAS float* wp = (const GAS float*)w.W + (size_t)(64 * w.kb + (lane >> 5)) * w.N + w.c0 + ccl;
; #pragma unroll
;     for (int i = 0; i < 32; ++i) v[i] = wp[(size_t)(2 * i) * w.N];
; }
; DI void w_tickets(LAS unsigned char* lds, const Ctx& c, int l, int budget) {
;     ...
;         if (i1 < W_NITEMS) { wb = w_decode(c, l, i1); w_load(wb, lane, vb); }
.LBB0_104:
	s_waitcnt vmcnt(0)
	v_lshl_or_b32 v2, s84, 6, v39
	v_cmp_gt_u32_e32 vcc, s89, v1
	v_mul_hi_u32_u24_e32 v3, s50, v2
	v_mul_u32_u24_e32 v2, s50, v2
	v_cndmask_b32_e32 v5, 0, v1, vcc
	v_lshl_add_u64 v[2:3], v[2:3], 2, s[74:75]
	s_ashr_i32 s61, s60, 31
	v_lshl_add_u64 v[2:3], s[60:61], 2, v[2:3]
	v_lshlrev_b32_e32 v48, 2, v5
	v_mov_b32_e32 v49, v4
	v_lshl_add_u64 v[2:3], v[2:3], 0, v[48:49]
	s_lshl_b32 s68, s50, 3
	v_lshl_add_u64 v[48:49], v[2:3], 0, s[68:69]
	v_lshl_add_u64 v[50:51], v[48:49], 0, s[68:69]
	v_lshl_add_u64 v[52:53], v[50:51], 0, s[68:69]
	v_lshl_add_u64 v[54:55], v[52:53], 0, s[68:69]
	v_lshl_add_u64 v[56:57], v[54:55], 0, s[68:69]
	v_lshl_add_u64 v[58:59], v[56:57], 0, s[68:69]
	global_load_dword v2, v[2:3], off nt
	s_nop 0
	global_load_dword v3, v[48:49], off nt
	global_load_dword v5, v[50:51], off nt
	s_nop 0
	global_load_dword v48, v[52:53], off nt
	global_load_dword v49, v[54:55], off nt
	global_load_dword v50, v[56:57], off nt
	global_load_dword v51, v[58:59], off nt
	v_lshl_add_u64 v[54:55], v[58:59], 0, s[68:69]
	global_load_dword v52, v[54:55], off nt
	v_lshl_add_u64 v[54:55], v[54:55], 0, s[68:69]
	v_lshl_add_u64 v[56:57], v[54:55], 0, s[68:69]
	global_load_dword v53, v[54:55], off nt
	s_nop 0
	global_load_dword v54, v[56:57], off nt
	v_lshl_add_u64 v[56:57], v[56:57], 0, s[68:69]
	v_lshl_add_u64 v[58:59], v[56:57], 0, s[68:69]
	global_load_dword v55, v[56:57], off nt
	s_nop 0
	global_load_dword v56, v[58:59], off nt
	v_lshl_add_u64 v[58:59], v[58:59], 0, s[68:69]
	v_lshl_add_u64 v[60:61], v[58:59], 0, s[68:69]
	global_load_dword v57, v[58:59], off nt
	s_nop 0
	global_load_dword v58, v[60:61], off nt
	v_lshl_add_u64 v[60:61], v[60:61], 0, s[68:69]
	v_lshl_add_u64 v[62:63], v[60:61], 0, s[68:69]
	global_load_dword v59, v[60:61], off nt
	s_nop 0
	global_load_dword v60, v[62:63], off nt
	v_lshl_add_u64 v[62:63], v[62:63], 0, s[68:69]
	v_lshl_add_u64 v[64:65], v[62:63], 0, s[68:69]
	global_load_dword v61, v[62:63], off nt
	s_nop 0
	global_load_dword v62, v[64:65], off nt
	v_lshl_add_u64 v[64:65], v[64:65], 0, s[68:69]
	v_lshl_add_u64 v[66:67], v[64:65], 0, s[68:69]
	global_load_dword v63, v[64:65], off nt
	s_nop 0
	global_load_dword v64, v[66:67], off nt
	v_lshl_add_u64 v[66:67], v[66:67], 0, s[68:69]
	v_lshl_add_u64 v[68:69], v[66:67], 0, s[68:69]
	global_load_dword v65, v[66:67], off nt
	s_nop 0
	global_load_dword v66, v[68:69], off nt
	v_lshl_add_u64 v[68:69], v[68:69], 0, s[68:69]
	v_lshl_add_u64 v[70:71], v[68:69], 0, s[68:69]
	global_load_dword v67, v[68:69], off nt
	s_nop 0
	global_load_dword v68, v[70:71], off nt
	v_lshl_add_u64 v[70:71], v[70:71], 0, s[68:69]
	v_lshl_add_u64 v[72:73], v[70:71], 0, s[68:69]
	global_load_dword v69, v[70:71], off nt
	s_nop 0
	global_load_dword v70, v[72:73], off nt
	v_lshl_add_u64 v[72:73], v[72:73], 0, s[68:69]
	v_lshl_add_u64 v[74:75], v[72:73], 0, s[68:69]
	global_load_dword v71, v[72:73], off nt
	s_nop 0
	global_load_dword v72, v[74:75], off nt
	v_lshl_add_u64 v[74:75], v[74:75], 0, s[68:69]
	v_lshl_add_u64 v[76:77], v[74:75], 0, s[68:69]
	global_load_dword v73, v[74:75], off nt
	s_nop 0
	global_load_dword v74, v[76:77], off nt
	v_lshl_add_u64 v[76:77], v[76:77], 0, s[68:69]
	global_load_dword v75, v[76:77], off nt
	v_lshl_add_u64 v[76:77], v[76:77], 0, s[68:69]
	global_load_dword v76, v[76:77], off nt

; #define GAS __attribute__((address_space(1)))
; DI void w_load(const WItem& w, int lane, float (&v)[32]) {
;     const int cc = lane & 31, ccl = cc < w.nv ? cc : 0; const GAS float* wp = (const GAS float*)w.W + (size_t)(64 * w.kb + (lane >> 5)) * w.N + w.c0 + ccl;
; #pragma unroll
;     for (int i = 0; i < 32; ++i) v[i] = wp[(size_t)(2 * i) * w.N];
; }
; DI void w_tickets(LAS unsigned char* lds, const Ctx& c, int l, int budget) {
;     ...
;         if (i2 < W_NITEMS) { wa = w_decode(c, l, i2); w_load(wa, lane, va); }
.LBB0_155:
	s_waitcnt vmcnt(0)
	v_lshl_or_b32 v6, s86, 6, v39
	v_cmp_gt_u32_e32 vcc, s87, v1
	v_mul_hi_u32_u24_e32 v7, s50, v6
	v_mul_u32_u24_e32 v6, s50, v6
	v_cndmask_b32_e32 v8, 0, v1, vcc
	v_lshl_add_u64 v[6:7], v[6:7], 2, s[74:75]
	s_ashr_i32 s61, s60, 31
	v_lshl_add_u64 v[6:7], s[60:61], 2, v[6:7]
	v_lshlrev_b32_e32 v8, 2, v8
	v_mov_b32_e32 v9, v4
	v_lshl_add_u64 v[6:7], v[6:7], 0, v[8:9]
	s_lshl_b32 s68, s50, 3
	v_lshl_add_u64 v[8:9], v[6:7], 0, s[68:69]
	v_lshl_add_u64 v[10:11], v[8:9], 0, s[68:69]
	v_lshl_add_u64 v[12:13], v[10:11], 0, s[68:69]
	v_lshl_add_u64 v[14:15], v[12:13], 0, s[68:69]
	v_lshl_add_u64 v[16:17], v[14:15], 0, s[68:69]
	v_lshl_add_u64 v[18:19], v[16:17], 0, s[68:69]
	global_load_dword v6, v[6:7], off nt
	s_nop 0
	global_load_dword v7, v[8:9], off nt
	s_nop 0
	global_load_dword v8, v[10:11], off nt
	global_load_dword v9, v[12:13], off nt
	s_nop 0
	global_load_dword v10, v[14:15], off nt
	global_load_dword v11, v[16:17], off nt
	global_load_dword v12, v[18:19], off nt
	v_lshl_add_u64 v[14:15], v[18:19], 0, s[68:69]
	v_lshl_add_u64 v[16:17], v[14:15], 0, s[68:69]
	global_load_dword v13, v[14:15], off nt
	s_nop 0
	global_load_dword v14, v[16:17], off nt
	v_lshl_add_u64 v[16:17], v[16:17], 0, s[68:69]
	v_lshl_add_u64 v[18:19], v[16:17], 0, s[68:69]
	global_load_dword v15, v[16:17], off nt
	s_nop 0
	global_load_dword v16, v[18:19], off nt
	v_lshl_add_u64 v[18:19], v[18:19], 0, s[68:69]
	v_lshl_add_u64 v[20:21], v[18:19], 0, s[68:69]
	global_load_dword v17, v[18:19], off nt
	s_nop 0
	global_load_dword v18, v[20:21], off nt
	v_lshl_add_u64 v[20:21], v[20:21], 0, s[68:69]
	v_lshl_add_u64 v[22:23], v[20:21], 0, s[68:69]
	global_load_dword v19, v[20:21], off nt
	s_nop 0
	global_load_dword v20, v[22:23], off nt
	v_lshl_add_u64 v[22:23], v[22:23], 0, s[68:69]
	v_lshl_add_u64 v[24:25], v[22:23], 0, s[68:69]
	global_load_dword v21, v[22:23], off nt
	s_nop 0
	global_load_dword v22, v[24:25], off nt
	v_lshl_add_u64 v[24:25], v[24:25], 0, s[68:69]
	v_lshl_add_u64 v[26:27], v[24:25], 0, s[68:69]
	global_load_dword v23, v[24:25], off nt
	s_nop 0
	global_load_dword v24, v[26:27], off nt
	v_lshl_add_u64 v[26:27], v[26:27], 0, s[68:69]
	v_lshl_add_u64 v[28:29], v[26:27], 0, s[68:69]
	global_load_dword v25, v[26:27], off nt
	s_nop 0
	global_load_dword v26, v[28:29], off nt
	v_lshl_add_u64 v[28:29], v[28:29], 0, s[68:69]
	v_lshl_add_u64 v[30:31], v[28:29], 0, s[68:69]
	global_load_dword v27, v[28:29], off nt
	s_nop 0
	global_load_dword v28, v[30:31], off nt
	v_lshl_add_u64 v[30:31], v[30:31], 0, s[68:69]
	v_lshl_add_u64 v[32:33], v[30:31], 0, s[68:69]
	global_load_dword v29, v[30:31], off nt
	s_nop 0
	global_load_dword v30, v[32:33], off nt
	v_lshl_add_u64 v[32:33], v[32:33], 0, s[68:69]
	v_lshl_add_u64 v[34:35], v[32:33], 0, s[68:69]
	global_load_dword v31, v[32:33], off nt
	s_nop 0
	global_load_dword v32, v[34:35], off nt
	v_lshl_add_u64 v[34:35], v[34:35], 0, s[68:69]
	v_lshl_add_u64 v[36:37], v[34:35], 0, s[68:69]
	global_load_dword v33, v[34:35], off nt
	s_nop 0
	global_load_dword v34, v[36:37], off nt
	v_lshl_add_u64 v[36:37], v[36:37], 0, s[68:69]
	v_lshl_add_u64 v[84:85], v[36:37], 0, s[68:69]
	global_load_dword v35, v[36:37], off nt
	s_nop 0
	global_load_dword v36, v[84:85], off nt
	v_lshl_add_u64 v[84:85], v[84:85], 0, s[68:69]
	global_load_dword v37, v[84:85], off nt
	s_andn2_b64 vcc, exec, s[42:43]
	s_cbranch_vccz .LBB0_108

; #define GAS __attribute__((address_space(1)))
; DI void w_load(const WItem& w, int lane, float (&v)[32]) {
;     const int cc = lane & 31, ccl = cc < w.nv ? cc : 0; const GAS float* wp = (const GAS float*)w.W + (size_t)(64 * w.kb + (lane >> 5)) * w.N + w.c0 + ccl;
; #pragma unroll
;     for (int i = 0; i < 32; ++i) v[i] = wp[(size_t)(2 * i) * w.N];
; }
; DI void w_tickets(LAS unsigned char* lds, const Ctx& c, int l, int budget) {
;     ...
;         if (i3 < W_NITEMS) { wb = w_decode(c, l, i3); w_load(wb, lane, vb); }
.LBB0_200:
	s_waitcnt vmcnt(0)
	v_lshl_or_b32 v2, s84, 6, v39
	v_cmp_gt_u32_e32 vcc, s89, v1
	v_mul_hi_u32_u24_e32 v3, s50, v2
	v_mul_u32_u24_e32 v2, s50, v2
	v_cndmask_b32_e32 v5, 0, v1, vcc
	v_lshl_add_u64 v[2:3], v[2:3], 2, s[74:75]
	s_ashr_i32 s61, s60, 31
	v_lshl_add_u64 v[2:3], s[60:61], 2, v[2:3]
	v_lshlrev_b32_e32 v48, 2, v5
	v_mov_b32_e32 v49, v4
	v_lshl_add_u64 v[2:3], v[2:3], 0, v[48:49]
	s_lshl_b32 s68, s50, 3
	v_lshl_add_u64 v[48:49], v[2:3], 0, s[68:69]
	v_lshl_add_u64 v[50:51], v[48:49], 0, s[68:69]
	v_lshl_add_u64 v[52:53], v[50:51], 0, s[68:69]
	v_lshl_add_u64 v[54:55], v[52:53], 0, s[68:69]
	v_lshl_add_u64 v[56:57], v[54:55], 0, s[68:69]
	v_lshl_add_u64 v[58:59], v[56:57], 0, s[68:69]
	global_load_dword v2, v[2:3], off nt
	s_nop 0
	global_load_dword v3, v[48:49], off nt
	global_load_dword v5, v[50:51], off nt
	s_nop 0
	global_load_dword v48, v[52:53], off nt
	global_load_dword v49, v[54:55], off nt
	global_load_dword v50, v[56:57], off nt
	global_load_dword v51, v[58:59], off nt
	v_lshl_add_u64 v[54:55], v[58:59], 0, s[68:69]
	global_load_dword v52, v[54:55], off nt
	v_lshl_add_u64 v[54:55], v[54:55], 0, s[68:69]
	v_lshl_add_u64 v[56:57], v[54:55], 0, s[68:69]
	global_load_dword v53, v[54:55], off nt
	s_nop 0
	global_load_dword v54, v[56:57], off nt
	v_lshl_add_u64 v[56:57], v[56:57], 0, s[68:69]
	v_lshl_add_u64 v[58:59], v[56:57], 0, s[68:69]
	global_load_dword v55, v[56:57], off nt
	s_nop 0
	global_load_dword v56, v[58:59], off nt
	v_lshl_add_u64 v[58:59], v[58:59], 0, s[68:69]
	v_lshl_add_u64 v[60:61], v[58:59], 0, s[68:69]
	global_load_dword v57, v[58:59], off nt
	s_nop 0
	global_load_dword v58, v[60:61], off nt
	v_lshl_add_u64 v[60:61], v[60:61], 0, s[68:69]
	v_lshl_add_u64 v[62:63], v[60:61], 0, s[68:69]
	global_load_dword v59, v[60:61], off nt
	s_nop 0
	global_load_dword v60, v[62:63], off nt
	v_lshl_add_u64 v[62:63], v[62:63], 0, s[68:69]
	v_lshl_add_u64 v[64:65], v[62:63], 0, s[68:69]
	global_load_dword v61, v[62:63], off nt
	s_nop 0
	global_load_dword v62, v[64:65], off nt
	v_lshl_add_u64 v[64:65], v[64:65], 0, s[68:69]
	v_lshl_add_u64 v[66:67], v[64:65], 0, s[68:69]
	global_load_dword v63, v[64:65], off nt
	s_nop 0
	global_load_dword v64, v[66:67], off nt
	v_lshl_add_u64 v[66:67], v[66:67], 0, s[68:69]
	v_lshl_add_u64 v[68:69], v[66:67], 0, s[68:69]
	global_load_dword v65, v[66:67], off nt
	s_nop 0
	global_load_dword v66, v[68:69], off nt
	v_lshl_add_u64 v[68:69], v[68:69], 0, s[68:69]
	v_lshl_add_u64 v[70:71], v[68:69], 0, s[68:69]
	global_load_dword v67, v[68:69], off nt
	s_nop 0
	global_load_dword v68, v[70:71], off nt
	v_lshl_add_u64 v[70:71], v[70:71], 0, s[68:69]
	v_lshl_add_u64 v[72:73], v[70:71], 0, s[68:69]
	global_load_dword v69, v[70:71], off nt
	s_nop 0
	global_load_dword v70, v[72:73], off nt
	v_lshl_add_u64 v[72:73], v[72:73], 0, s[68:69]
	v_lshl_add_u64 v[74:75], v[72:73], 0, s[68:69]
	global_load_dword v71, v[72:73], off nt
	s_nop 0
	global_load_dword v72, v[74:75], off nt
	v_lshl_add_u64 v[74:75], v[74:75], 0, s[68:69]
	v_lshl_add_u64 v[84:85], v[74:75], 0, s[68:69]
	global_load_dword v73, v[74:75], off nt
	s_nop 0
	global_load_dword v74, v[84:85], off nt
	v_lshl_add_u64 v[84:85], v[84:85], 0, s[68:69]
	global_load_dword v75, v[84:85], off nt
	v_lshl_add_u64 v[84:85], v[84:85], 0, s[68:69]
	global_load_dword v76, v[84:85], off nt
	s_andn2_b64 vcc, exec, s[58:59]
	s_cbranch_vccz .LBB0_110

; #define GAS __attribute__((address_space(1)))
; DI void w_load(const WItem& w, int lane, float (&v)[32]) {
;     const int cc = lane & 31, ccl = cc < w.nv ? cc : 0; const GAS float* wp = (const GAS float*)w.W + (size_t)(64 * w.kb + (lane >> 5)) * w.N + w.c0 + ccl;
; #pragma unroll
;     for (int i = 0; i < 32; ++i) v[i] = wp[(size_t)(2 * i) * w.N];
; }
; DI void w_tickets(LAS unsigned char* lds, const Ctx& c, int l, int budget) {
;     ...
;         if (i0 < W_NITEMS) { wa = w_decode(c, l, i0); w_load(wa, lane, va); }
.LBB0_371:
	v_lshl_or_b32 v2, s87, 6, v40
	v_cmp_gt_u32_e32 vcc, s76, v1
	v_mul_hi_u32_u24_e32 v3, s60, v2
	v_mul_u32_u24_e32 v2, s60, v2
	v_cndmask_b32_e32 v5, 0, v1, vcc
	v_lshl_add_u64 v[2:3], v[2:3], 2, s[56:57]
	s_ashr_i32 s55, s54, 31
	v_lshl_add_u64 v[2:3], s[54:55], 2, v[2:3]
	v_lshlrev_b32_e32 v6, 2, v5
	v_mov_b32_e32 v7, v4
	s_mov_b32 s2, s68
	v_lshl_add_u64 v[2:3], v[2:3], 0, v[6:7]
	s_lshl_b32 s68, s60, 3
	global_load_dword v6, v[2:3], off nt
	v_lshl_add_u64 v[2:3], v[2:3], 0, s[68:69]
	global_load_dword v7, v[2:3], off nt
	v_lshl_add_u64 v[2:3], v[2:3], 0, s[68:69]
	global_load_dword v8, v[2:3], off nt
	v_lshl_add_u64 v[2:3], v[2:3], 0, s[68:69]
	global_load_dword v9, v[2:3], off nt
	v_lshl_add_u64 v[2:3], v[2:3], 0, s[68:69]
	global_load_dword v10, v[2:3], off nt
	v_lshl_add_u64 v[2:3], v[2:3], 0, s[68:69]
	global_load_dword v11, v[2:3], off nt
	v_lshl_add_u64 v[2:3], v[2:3], 0, s[68:69]
	global_load_dword v12, v[2:3], off nt
	v_lshl_add_u64 v[2:3], v[2:3], 0, s[68:69]
	global_load_dword v13, v[2:3], off nt
	v_lshl_add_u64 v[2:3], v[2:3], 0, s[68:69]
	global_load_dword v14, v[2:3], off nt
	v_lshl_add_u64 v[2:3], v[2:3], 0, s[68:69]
	global_load_dword v15, v[2:3], off nt
	v_lshl_add_u64 v[2:3], v[2:3], 0, s[68:69]
	global_load_dword v16, v[2:3], off nt
	v_lshl_add_u64 v[2:3], v[2:3], 0, s[68:69]
	global_load_dword v17, v[2:3], off nt
	v_lshl_add_u64 v[2:3], v[2:3], 0, s[68:69]
	global_load_dword v18, v[2:3], off nt
	v_lshl_add_u64 v[2:3], v[2:3], 0, s[68:69]
	global_load_dword v19, v[2:3], off nt
	v_lshl_add_u64 v[2:3], v[2:3], 0, s[68:69]
	global_load_dword v20, v[2:3], off nt
	v_lshl_add_u64 v[2:3], v[2:3], 0, s[68:69]
	global_load_dword v21, v[2:3], off nt
	v_lshl_add_u64 v[2:3], v[2:3], 0, s[68:69]
	global_load_dword v22, v[2:3], off nt
	v_lshl_add_u64 v[2:3], v[2:3], 0, s[68:69]
	global_load_dword v23, v[2:3], off nt
	v_lshl_add_u64 v[2:3], v[2:3], 0, s[68:69]
	global_load_dword v24, v[2:3], off nt
	v_lshl_add_u64 v[2:3], v[2:3], 0, s[68:69]
	global_load_dword v25, v[2:3], off nt
	v_lshl_add_u64 v[2:3], v[2:3], 0, s[68:69]
	global_load_dword v26, v[2:3], off nt
	v_lshl_add_u64 v[2:3], v[2:3], 0, s[68:69]
	global_load_dword v27, v[2:3], off nt
	v_lshl_add_u64 v[2:3], v[2:3], 0, s[68:69]
	global_load_dword v28, v[2:3], off nt
	v_lshl_add_u64 v[2:3], v[2:3], 0, s[68:69]
	global_load_dword v29, v[2:3], off nt
	v_lshl_add_u64 v[2:3], v[2:3], 0, s[68:69]
	global_load_dword v30, v[2:3], off nt
	v_lshl_add_u64 v[2:3], v[2:3], 0, s[68:69]
	global_load_dword v31, v[2:3], off nt
	v_lshl_add_u64 v[2:3], v[2:3], 0, s[68:69]
	global_load_dword v32, v[2:3], off nt
	v_lshl_add_u64 v[2:3], v[2:3], 0, s[68:69]
	global_load_dword v33, v[2:3], off nt
	v_lshl_add_u64 v[2:3], v[2:3], 0, s[68:69]
	global_load_dword v34, v[2:3], off nt
	v_lshl_add_u64 v[2:3], v[2:3], 0, s[68:69]
	global_load_dword v35, v[2:3], off nt
	v_lshl_add_u64 v[2:3], v[2:3], 0, s[68:69]
	global_load_dword v36, v[2:3], off nt
	v_lshl_add_u64 v[2:3], v[2:3], 0, s[68:69]
	global_load_dword v37, v[2:3], off nt
	s_mov_b32 s68, s2
	s_cmpk_lt_i32 s53, 0x7878
	s_cselect_b64 s[56:57], -1, 0
	s_cmpk_gt_i32 s53, 0x7877
	s_cbranch_scc1 .LBB0_416

; #define GAS __attribute__((address_space(1)))
; DI void w_load(const WItem& w, int lane, float (&v)[32]) {
;     const int cc = lane & 31, ccl = cc < w.nv ? cc : 0; const GAS float* wp = (const GAS float*)w.W + (size_t)(64 * w.kb + (lane >> 5)) * w.N + w.c0 + ccl;
; #pragma unroll
;     for (int i = 0; i < 32; ++i) v[i] = wp[(size_t)(2 * i) * w.N];
; }
; DI void w_tickets(LAS unsigned char* lds, const Ctx& c, int l, int budget) {
;     ...
;         if (i1 < W_NITEMS) { wb = w_decode(c, l, i1); w_load(wb, lane, vb); }
.LBB0_415:
	v_lshl_or_b32 v2, s82, 6, v40
	v_cmp_gt_u32_e32 vcc, s83, v1
	v_mul_hi_u32_u24_e32 v3, s66, v2
	v_mul_u32_u24_e32 v2, s66, v2
	v_cndmask_b32_e32 v5, 0, v1, vcc
	v_lshl_add_u64 v[2:3], v[2:3], 2, s[62:63]
	s_ashr_i32 s61, s60, 31
	v_lshl_add_u64 v[2:3], s[60:61], 2, v[2:3]
	v_lshlrev_b32_e32 v44, 2, v5
	v_mov_b32_e32 v45, v4
	s_mov_b32 s2, s68
	v_lshl_add_u64 v[2:3], v[2:3], 0, v[44:45]
	s_lshl_b32 s68, s66, 3
	global_load_dword v51, v[2:3], off nt
	v_lshl_add_u64 v[2:3], v[2:3], 0, s[68:69]
	global_load_dword v52, v[2:3], off nt
	v_lshl_add_u64 v[2:3], v[2:3], 0, s[68:69]
	global_load_dword v53, v[2:3], off nt
	v_lshl_add_u64 v[2:3], v[2:3], 0, s[68:69]
	global_load_dword v54, v[2:3], off nt
	v_lshl_add_u64 v[2:3], v[2:3], 0, s[68:69]
	global_load_dword v55, v[2:3], off nt
	v_lshl_add_u64 v[2:3], v[2:3], 0, s[68:69]
	global_load_dword v56, v[2:3], off nt
	v_lshl_add_u64 v[2:3], v[2:3], 0, s[68:69]
	global_load_dword v57, v[2:3], off nt
	v_lshl_add_u64 v[2:3], v[2:3], 0, s[68:69]
	global_load_dword v58, v[2:3], off nt
	v_lshl_add_u64 v[2:3], v[2:3], 0, s[68:69]
	global_load_dword v59, v[2:3], off nt
	v_lshl_add_u64 v[2:3], v[2:3], 0, s[68:69]
	global_load_dword v60, v[2:3], off nt
	v_lshl_add_u64 v[2:3], v[2:3], 0, s[68:69]
	global_load_dword v61, v[2:3], off nt
	v_lshl_add_u64 v[2:3], v[2:3], 0, s[68:69]
	global_load_dword v62, v[2:3], off nt
	v_lshl_add_u64 v[2:3], v[2:3], 0, s[68:69]
	global_load_dword v63, v[2:3], off nt
	v_lshl_add_u64 v[2:3], v[2:3], 0, s[68:69]
	global_load_dword v64, v[2:3], off nt
	v_lshl_add_u64 v[2:3], v[2:3], 0, s[68:69]
	global_load_dword v65, v[2:3], off nt
	v_lshl_add_u64 v[2:3], v[2:3], 0, s[68:69]
	global_load_dword v66, v[2:3], off nt
	v_lshl_add_u64 v[2:3], v[2:3], 0, s[68:69]
	global_load_dword v67, v[2:3], off nt
	v_lshl_add_u64 v[2:3], v[2:3], 0, s[68:69]
	global_load_dword v68, v[2:3], off nt
	v_lshl_add_u64 v[2:3], v[2:3], 0, s[68:69]
	global_load_dword v69, v[2:3], off nt
	v_lshl_add_u64 v[2:3], v[2:3], 0, s[68:69]
	global_load_dword v70, v[2:3], off nt
	v_lshl_add_u64 v[2:3], v[2:3], 0, s[68:69]
	global_load_dword v71, v[2:3], off nt
	v_lshl_add_u64 v[2:3], v[2:3], 0, s[68:69]
	global_load_dword v72, v[2:3], off nt
	v_lshl_add_u64 v[2:3], v[2:3], 0, s[68:69]
	global_load_dword v73, v[2:3], off nt
	v_lshl_add_u64 v[2:3], v[2:3], 0, s[68:69]
	global_load_dword v74, v[2:3], off nt
	v_lshl_add_u64 v[2:3], v[2:3], 0, s[68:69]
	global_load_dword v75, v[2:3], off nt
	v_lshl_add_u64 v[2:3], v[2:3], 0, s[68:69]
	global_load_dword v76, v[2:3], off nt
	v_lshl_add_u64 v[2:3], v[2:3], 0, s[68:69]
	global_load_dword v77, v[2:3], off nt
	v_lshl_add_u64 v[2:3], v[2:3], 0, s[68:69]
	global_load_dword v78, v[2:3], off nt
	v_lshl_add_u64 v[2:3], v[2:3], 0, s[68:69]
	global_load_dword v79, v[2:3], off nt
	v_lshl_add_u64 v[2:3], v[2:3], 0, s[68:69]
	global_load_dword v80, v[2:3], off nt
	v_lshl_add_u64 v[2:3], v[2:3], 0, s[68:69]
	global_load_dword v81, v[2:3], off nt
	v_lshl_add_u64 v[2:3], v[2:3], 0, s[68:69]
	global_load_dword v82, v[2:3], off nt
	s_mov_b32 s68, s2

; #define GAS __attribute__((address_space(1)))
; DI void w_load(const WItem& w, int lane, float (&v)[32]) {
;     const int cc = lane & 31, ccl = cc < w.nv ? cc : 0; const GAS float* wp = (const GAS float*)w.W + (size_t)(64 * w.kb + (lane >> 5)) * w.N + w.c0 + ccl;
; #pragma unroll
;     for (int i = 0; i < 32; ++i) v[i] = wp[(size_t)(2 * i) * w.N];
; }
; DI void w_tickets(LAS unsigned char* lds, const Ctx& c, int l, int budget) {
;     ...
;         if (i2 < W_NITEMS) { wa = w_decode(c, l, i2); w_load(wa, lane, va); }
.LBB0_466:
	s_waitcnt vmcnt(31)
	v_lshl_or_b32 v6, s79, 6, v40
	v_cmp_gt_u32_e32 vcc, s76, v1
	s_waitcnt vmcnt(30)
	v_mul_hi_u32_u24_e32 v7, s66, v6
	v_mul_u32_u24_e32 v6, s66, v6
	s_waitcnt vmcnt(29)
	v_cndmask_b32_e32 v8, 0, v1, vcc
	v_lshl_add_u64 v[6:7], v[6:7], 2, s[62:63]
	s_ashr_i32 s61, s60, 31
	v_lshl_add_u64 v[6:7], s[60:61], 2, v[6:7]
	v_lshlrev_b32_e32 v8, 2, v8
	s_waitcnt vmcnt(28)
	v_mov_b32_e32 v9, v4
	v_lshl_add_u64 v[8:9], v[6:7], 0, v[8:9]
	s_lshl_b32 s68, s66, 3
	global_load_dword v6, v[8:9], off nt
	v_lshl_add_u64 v[8:9], v[8:9], 0, s[68:69]
	s_waitcnt vmcnt(27)
	v_lshl_add_u64 v[10:11], v[8:9], 0, s[68:69]
	global_load_dword v7, v[8:9], off nt
	s_mov_b32 s87, s79
	global_load_dword v8, v[10:11], off nt
	v_lshl_add_u64 v[10:11], v[10:11], 0, s[68:69]
	s_waitcnt vmcnt(27)
	v_lshl_add_u64 v[12:13], v[10:11], 0, s[68:69]
	global_load_dword v9, v[10:11], off nt
	s_nop 0
	global_load_dword v10, v[12:13], off nt
	v_lshl_add_u64 v[12:13], v[12:13], 0, s[68:69]
	s_waitcnt vmcnt(27)
	v_lshl_add_u64 v[14:15], v[12:13], 0, s[68:69]
	global_load_dword v11, v[12:13], off nt
	s_nop 0
	global_load_dword v12, v[14:15], off nt
	v_lshl_add_u64 v[14:15], v[14:15], 0, s[68:69]
	s_waitcnt vmcnt(27)
	v_lshl_add_u64 v[16:17], v[14:15], 0, s[68:69]
	global_load_dword v13, v[14:15], off nt
	s_nop 0
	global_load_dword v14, v[16:17], off nt
	v_lshl_add_u64 v[16:17], v[16:17], 0, s[68:69]
	s_waitcnt vmcnt(27)
	v_lshl_add_u64 v[18:19], v[16:17], 0, s[68:69]
	global_load_dword v15, v[16:17], off nt
	s_nop 0
	global_load_dword v16, v[18:19], off nt
	v_lshl_add_u64 v[18:19], v[18:19], 0, s[68:69]
	s_waitcnt vmcnt(27)
	v_lshl_add_u64 v[20:21], v[18:19], 0, s[68:69]
	global_load_dword v17, v[18:19], off nt
	s_nop 0
	global_load_dword v18, v[20:21], off nt
	v_lshl_add_u64 v[20:21], v[20:21], 0, s[68:69]
	s_waitcnt vmcnt(27)
	v_lshl_add_u64 v[22:23], v[20:21], 0, s[68:69]
	global_load_dword v19, v[20:21], off nt
	s_nop 0
	global_load_dword v20, v[22:23], off nt
	v_lshl_add_u64 v[22:23], v[22:23], 0, s[68:69]
	s_waitcnt vmcnt(27)
	v_lshl_add_u64 v[24:25], v[22:23], 0, s[68:69]
	global_load_dword v21, v[22:23], off nt
	s_nop 0
	global_load_dword v22, v[24:25], off nt
	v_lshl_add_u64 v[24:25], v[24:25], 0, s[68:69]
	s_waitcnt vmcnt(27)
	v_lshl_add_u64 v[26:27], v[24:25], 0, s[68:69]
	global_load_dword v23, v[24:25], off nt
	s_nop 0
	global_load_dword v24, v[26:27], off nt
	v_lshl_add_u64 v[26:27], v[26:27], 0, s[68:69]
	s_waitcnt vmcnt(27)
	v_lshl_add_u64 v[28:29], v[26:27], 0, s[68:69]
	global_load_dword v25, v[26:27], off nt
	s_nop 0
	global_load_dword v26, v[28:29], off nt
	v_lshl_add_u64 v[28:29], v[28:29], 0, s[68:69]
	s_waitcnt vmcnt(27)
	v_lshl_add_u64 v[30:31], v[28:29], 0, s[68:69]
	global_load_dword v27, v[28:29], off nt
	s_nop 0
	global_load_dword v28, v[30:31], off nt
	v_lshl_add_u64 v[30:31], v[30:31], 0, s[68:69]
	s_waitcnt vmcnt(27)
	v_lshl_add_u64 v[32:33], v[30:31], 0, s[68:69]
	global_load_dword v29, v[30:31], off nt
	s_nop 0
	global_load_dword v30, v[32:33], off nt
	v_lshl_add_u64 v[32:33], v[32:33], 0, s[68:69]
	s_waitcnt vmcnt(27)
	v_lshl_add_u64 v[34:35], v[32:33], 0, s[68:69]
	global_load_dword v31, v[32:33], off nt
	s_nop 0
	global_load_dword v32, v[34:35], off nt
	v_lshl_add_u64 v[34:35], v[34:35], 0, s[68:69]
	s_waitcnt vmcnt(27)
	v_lshl_add_u64 v[36:37], v[34:35], 0, s[68:69]
	global_load_dword v33, v[34:35], off nt
	s_nop 0
	global_load_dword v34, v[36:37], off nt
	v_lshl_add_u64 v[36:37], v[36:37], 0, s[68:69]
	v_lshl_add_u64 v[84:85], v[36:37], 0, s[68:69]
	global_load_dword v35, v[36:37], off nt
	s_nop 0
	global_load_dword v36, v[84:85], off nt
	v_lshl_add_u64 v[84:85], v[84:85], 0, s[68:69]
	global_load_dword v37, v[84:85], off nt
	s_andn2_b64 vcc, exec, s[56:57]
	s_cbranch_vccz .LBB0_462

; #define GAS __attribute__((address_space(1)))
; DI void w_load(const WItem& w, int lane, float (&v)[32]) {
;     const int cc = lane & 31, ccl = cc < w.nv ? cc : 0; const GAS float* wp = (const GAS float*)w.W + (size_t)(64 * w.kb + (lane >> 5)) * w.N + w.c0 + ccl;
; #pragma unroll
;     for (int i = 0; i < 32; ++i) v[i] = wp[(size_t)(2 * i) * w.N];
; }
; DI void w_tickets(LAS unsigned char* lds, const Ctx& c, int l, int budget) {
;     ...
;         if (i3 < W_NITEMS) { wb = w_decode(c, l, i3); w_load(wb, lane, vb); }
.LBB0_511:
	v_lshl_or_b32 v40, s82, 6, v40
	v_cmp_gt_u32_e32 vcc, s83, v1
	s_waitcnt vmcnt(29)
	v_mul_hi_u32_u24_e32 v53, s30, v40
	v_mul_u32_u24_e32 v52, s30, v40
	v_cndmask_b32_e32 v51, 0, v1, vcc
	v_lshl_add_u64 v[52:53], v[52:53], 2, s[16:17]
	s_ashr_i32 s55, s54, 31
	v_lshl_add_u64 v[52:53], s[54:55], 2, v[52:53]
	s_waitcnt vmcnt(28)
	v_lshlrev_b32_e32 v54, 2, v51
	s_waitcnt vmcnt(27)
	v_mov_b32_e32 v55, v4
	v_lshl_add_u64 v[52:53], v[52:53], 0, v[54:55]
	s_lshl_b32 s68, s30, 3
	v_lshl_add_u64 v[54:55], v[52:53], 0, s[68:69]
	global_load_dword v51, v[52:53], off nt
	s_mov_b64 s[54:55], s[0:1]
	global_load_dword v52, v[54:55], off nt
	v_lshl_add_u64 v[54:55], v[54:55], 0, s[68:69]
	s_waitcnt vmcnt(27)
	v_lshl_add_u64 v[56:57], v[54:55], 0, s[68:69]
	global_load_dword v53, v[54:55], off nt
	s_nop 0
	global_load_dword v54, v[56:57], off nt
	v_lshl_add_u64 v[56:57], v[56:57], 0, s[68:69]
	s_waitcnt vmcnt(27)
	v_lshl_add_u64 v[58:59], v[56:57], 0, s[68:69]
	global_load_dword v55, v[56:57], off nt
	s_nop 0
	global_load_dword v56, v[58:59], off nt
	v_lshl_add_u64 v[58:59], v[58:59], 0, s[68:69]
	s_waitcnt vmcnt(27)
	v_lshl_add_u64 v[60:61], v[58:59], 0, s[68:69]
	global_load_dword v57, v[58:59], off nt
	s_nop 0
	global_load_dword v58, v[60:61], off nt
	v_lshl_add_u64 v[60:61], v[60:61], 0, s[68:69]
	s_waitcnt vmcnt(27)
	v_lshl_add_u64 v[62:63], v[60:61], 0, s[68:69]
	global_load_dword v59, v[60:61], off nt
	s_nop 0
	global_load_dword v60, v[62:63], off nt
	v_lshl_add_u64 v[62:63], v[62:63], 0, s[68:69]
	s_waitcnt vmcnt(27)
	v_lshl_add_u64 v[64:65], v[62:63], 0, s[68:69]
	global_load_dword v61, v[62:63], off nt
	s_nop 0
	global_load_dword v62, v[64:65], off nt
	v_lshl_add_u64 v[64:65], v[64:65], 0, s[68:69]
	s_waitcnt vmcnt(27)
	v_lshl_add_u64 v[66:67], v[64:65], 0, s[68:69]
	global_load_dword v63, v[64:65], off nt
	s_nop 0
	global_load_dword v64, v[66:67], off nt
	v_lshl_add_u64 v[66:67], v[66:67], 0, s[68:69]
	s_waitcnt vmcnt(27)
	v_lshl_add_u64 v[68:69], v[66:67], 0, s[68:69]
	global_load_dword v65, v[66:67], off nt
	s_nop 0
	global_load_dword v66, v[68:69], off nt
	v_lshl_add_u64 v[68:69], v[68:69], 0, s[68:69]
	s_waitcnt vmcnt(27)
	v_lshl_add_u64 v[70:71], v[68:69], 0, s[68:69]
	global_load_dword v67, v[68:69], off nt
	s_nop 0
	global_load_dword v68, v[70:71], off nt
	v_lshl_add_u64 v[70:71], v[70:71], 0, s[68:69]
	s_waitcnt vmcnt(27)
	v_lshl_add_u64 v[72:73], v[70:71], 0, s[68:69]
	global_load_dword v69, v[70:71], off nt
	s_nop 0
	global_load_dword v70, v[72:73], off nt
	v_lshl_add_u64 v[72:73], v[72:73], 0, s[68:69]
	s_waitcnt vmcnt(27)
	v_lshl_add_u64 v[74:75], v[72:73], 0, s[68:69]
	global_load_dword v71, v[72:73], off nt
	s_nop 0
	global_load_dword v72, v[74:75], off nt
	v_lshl_add_u64 v[74:75], v[74:75], 0, s[68:69]
	s_waitcnt vmcnt(27)
	v_lshl_add_u64 v[76:77], v[74:75], 0, s[68:69]
	global_load_dword v73, v[74:75], off nt
	s_nop 0
	global_load_dword v74, v[76:77], off nt
	v_lshl_add_u64 v[76:77], v[76:77], 0, s[68:69]
	s_waitcnt vmcnt(27)
	v_lshl_add_u64 v[78:79], v[76:77], 0, s[68:69]
	global_load_dword v75, v[76:77], off nt
	s_nop 0
	global_load_dword v76, v[78:79], off nt
	v_lshl_add_u64 v[78:79], v[78:79], 0, s[68:69]
	s_waitcnt vmcnt(27)
	v_lshl_add_u64 v[80:81], v[78:79], 0, s[68:69]
	global_load_dword v77, v[78:79], off nt
	s_nop 0
	global_load_dword v78, v[80:81], off nt
	v_lshl_add_u64 v[80:81], v[80:81], 0, s[68:69]
	s_waitcnt vmcnt(28)
	v_lshl_add_u64 v[82:83], v[80:81], 0, s[68:69]
	global_load_dword v79, v[80:81], off nt
	s_nop 0
	global_load_dword v80, v[82:83], off nt
	v_lshl_add_u64 v[82:83], v[82:83], 0, s[68:69]
	global_load_dword v81, v[82:83], off nt
	v_lshl_add_u64 v[82:83], v[82:83], 0, s[68:69]
	global_load_dword v82, v[82:83], off nt
	s_andn2_b64 vcc, exec, s[58:59]
	s_cbranch_vccz .LBB0_464

; #define GAS __attribute__((address_space(1)))
; DI void w_load(const WItem& w, int lane, float (&v)[32]) {
;     const int cc = lane & 31, ccl = cc < w.nv ? cc : 0; const GAS float* wp = (const GAS float*)w.W + (size_t)(64 * w.kb + (lane >> 5)) * w.N + w.c0 + ccl;
; #pragma unroll
;     for (int i = 0; i < 32; ++i) v[i] = wp[(size_t)(2 * i) * w.N];
; }
.LBB0_1431:
	v_lshl_or_b32 v2, s81, 6, v40
	v_cmp_gt_u32_e32 vcc, s78, v1
	v_mul_hi_u32_u24_e32 v3, s60, v2
	v_mul_u32_u24_e32 v2, s60, v2
	v_cndmask_b32_e32 v5, 0, v1, vcc
	v_lshl_add_u64 v[2:3], v[2:3], 2, s[56:57]
	s_ashr_i32 s55, s54, 31
	v_lshl_add_u64 v[2:3], s[54:55], 2, v[2:3]
	v_lshlrev_b32_e32 v6, 2, v5
	v_mov_b32_e32 v7, v4
	v_lshl_add_u64 v[2:3], v[2:3], 0, v[6:7]
	s_lshl_b32 s68, s60, 3
	global_load_dword v6, v[2:3], off nt
	v_lshl_add_u64 v[2:3], v[2:3], 0, s[68:69]
	global_load_dword v7, v[2:3], off nt
	v_lshl_add_u64 v[2:3], v[2:3], 0, s[68:69]
	global_load_dword v8, v[2:3], off nt
	v_lshl_add_u64 v[2:3], v[2:3], 0, s[68:69]
	global_load_dword v9, v[2:3], off nt
	v_lshl_add_u64 v[2:3], v[2:3], 0, s[68:69]
	global_load_dword v10, v[2:3], off nt
	v_lshl_add_u64 v[2:3], v[2:3], 0, s[68:69]
	global_load_dword v11, v[2:3], off nt
	v_lshl_add_u64 v[2:3], v[2:3], 0, s[68:69]
	global_load_dword v12, v[2:3], off nt
	v_lshl_add_u64 v[2:3], v[2:3], 0, s[68:69]
	global_load_dword v13, v[2:3], off nt
	v_lshl_add_u64 v[2:3], v[2:3], 0, s[68:69]
	global_load_dword v14, v[2:3], off nt
	v_lshl_add_u64 v[2:3], v[2:3], 0, s[68:69]
	global_load_dword v15, v[2:3], off nt
	v_lshl_add_u64 v[2:3], v[2:3], 0, s[68:69]
	global_load_dword v16, v[2:3], off nt
	v_lshl_add_u64 v[2:3], v[2:3], 0, s[68:69]
	global_load_dword v17, v[2:3], off nt
	v_lshl_add_u64 v[2:3], v[2:3], 0, s[68:69]
	global_load_dword v18, v[2:3], off nt
	v_lshl_add_u64 v[2:3], v[2:3], 0, s[68:69]
	global_load_dword v19, v[2:3], off nt
	v_lshl_add_u64 v[2:3], v[2:3], 0, s[68:69]
	global_load_dword v20, v[2:3], off nt
	v_lshl_add_u64 v[2:3], v[2:3], 0, s[68:69]
	global_load_dword v21, v[2:3], off nt
	v_lshl_add_u64 v[2:3], v[2:3], 0, s[68:69]
	global_load_dword v22, v[2:3], off nt
	v_lshl_add_u64 v[2:3], v[2:3], 0, s[68:69]
	global_load_dword v23, v[2:3], off nt
	v_lshl_add_u64 v[2:3], v[2:3], 0, s[68:69]
	global_load_dword v24, v[2:3], off nt
	v_lshl_add_u64 v[2:3], v[2:3], 0, s[68:69]
	global_load_dword v25, v[2:3], off nt
	v_lshl_add_u64 v[2:3], v[2:3], 0, s[68:69]
	global_load_dword v26, v[2:3], off nt
	v_lshl_add_u64 v[2:3], v[2:3], 0, s[68:69]
	global_load_dword v27, v[2:3], off nt
	v_lshl_add_u64 v[2:3], v[2:3], 0, s[68:69]
	global_load_dword v28, v[2:3], off nt
	v_lshl_add_u64 v[2:3], v[2:3], 0, s[68:69]
	global_load_dword v29, v[2:3], off nt
	v_lshl_add_u64 v[2:3], v[2:3], 0, s[68:69]
	global_load_dword v30, v[2:3], off nt
	v_lshl_add_u64 v[2:3], v[2:3], 0, s[68:69]
	global_load_dword v31, v[2:3], off nt
	v_lshl_add_u64 v[2:3], v[2:3], 0, s[68:69]
	global_load_dword v32, v[2:3], off nt
	v_lshl_add_u64 v[2:3], v[2:3], 0, s[68:69]
	global_load_dword v33, v[2:3], off nt
	v_lshl_add_u64 v[2:3], v[2:3], 0, s[68:69]
	global_load_dword v34, v[2:3], off nt
	v_lshl_add_u64 v[2:3], v[2:3], 0, s[68:69]
	global_load_dword v35, v[2:3], off nt
	v_lshl_add_u64 v[2:3], v[2:3], 0, s[68:69]
	global_load_dword v36, v[2:3], off nt
	v_lshl_add_u64 v[2:3], v[2:3], 0, s[68:69]
	global_load_dword v37, v[2:3], off nt
	s_cmpk_lt_i32 s76, 0x7878
	s_cselect_b64 s[56:57], -1, 0
	s_cmpk_gt_i32 s76, 0x7877
	s_cbranch_scc1 .LBB0_1476

; #define GAS __attribute__((address_space(1)))
; DI void w_load(const WItem& w, int lane, float (&v)[32]) {
;     const int cc = lane & 31, ccl = cc < w.nv ? cc : 0; const GAS float* wp = (const GAS float*)w.W + (size_t)(64 * w.kb + (lane >> 5)) * w.N + w.c0 + ccl;
; #pragma unroll
;     for (int i = 0; i < 32; ++i) v[i] = wp[(size_t)(2 * i) * w.N];
; }
.LBB0_1475:
	v_lshl_or_b32 v2, s83, 6, v40
	v_cmp_gt_u32_e32 vcc, s84, v1
	v_mul_hi_u32_u24_e32 v3, s66, v2
	v_mul_u32_u24_e32 v2, s66, v2
	v_cndmask_b32_e32 v5, 0, v1, vcc
	v_lshl_add_u64 v[2:3], v[2:3], 2, s[62:63]
	s_ashr_i32 s61, s60, 31
	v_lshl_add_u64 v[2:3], s[60:61], 2, v[2:3]
	v_lshlrev_b32_e32 v44, 2, v5
	v_mov_b32_e32 v45, v4
	v_lshl_add_u64 v[2:3], v[2:3], 0, v[44:45]
	s_lshl_b32 s68, s66, 3
	global_load_dword v51, v[2:3], off nt
	v_lshl_add_u64 v[2:3], v[2:3], 0, s[68:69]
	global_load_dword v52, v[2:3], off nt
	v_lshl_add_u64 v[2:3], v[2:3], 0, s[68:69]
	global_load_dword v53, v[2:3], off nt
	v_lshl_add_u64 v[2:3], v[2:3], 0, s[68:69]
	global_load_dword v54, v[2:3], off nt
	v_lshl_add_u64 v[2:3], v[2:3], 0, s[68:69]
	global_load_dword v55, v[2:3], off nt
	v_lshl_add_u64 v[2:3], v[2:3], 0, s[68:69]
	global_load_dword v56, v[2:3], off nt
	v_lshl_add_u64 v[2:3], v[2:3], 0, s[68:69]
	global_load_dword v57, v[2:3], off nt
	v_lshl_add_u64 v[2:3], v[2:3], 0, s[68:69]
	global_load_dword v58, v[2:3], off nt
	v_lshl_add_u64 v[2:3], v[2:3], 0, s[68:69]
	global_load_dword v59, v[2:3], off nt
	v_lshl_add_u64 v[2:3], v[2:3], 0, s[68:69]
	global_load_dword v60, v[2:3], off nt
	v_lshl_add_u64 v[2:3], v[2:3], 0, s[68:69]
	global_load_dword v61, v[2:3], off nt
	v_lshl_add_u64 v[2:3], v[2:3], 0, s[68:69]
	global_load_dword v62, v[2:3], off nt
	v_lshl_add_u64 v[2:3], v[2:3], 0, s[68:69]
	global_load_dword v63, v[2:3], off nt
	v_lshl_add_u64 v[2:3], v[2:3], 0, s[68:69]
	global_load_dword v64, v[2:3], off nt
	v_lshl_add_u64 v[2:3], v[2:3], 0, s[68:69]
	global_load_dword v65, v[2:3], off nt
	v_lshl_add_u64 v[2:3], v[2:3], 0, s[68:69]
	global_load_dword v66, v[2:3], off nt
	v_lshl_add_u64 v[2:3], v[2:3], 0, s[68:69]
	global_load_dword v67, v[2:3], off nt
	v_lshl_add_u64 v[2:3], v[2:3], 0, s[68:69]
	global_load_dword v68, v[2:3], off nt
	v_lshl_add_u64 v[2:3], v[2:3], 0, s[68:69]
	global_load_dword v69, v[2:3], off nt
	v_lshl_add_u64 v[2:3], v[2:3], 0, s[68:69]
	global_load_dword v70, v[2:3], off nt
	v_lshl_add_u64 v[2:3], v[2:3], 0, s[68:69]
	global_load_dword v71, v[2:3], off nt
	v_lshl_add_u64 v[2:3], v[2:3], 0, s[68:69]
	global_load_dword v72, v[2:3], off nt
	v_lshl_add_u64 v[2:3], v[2:3], 0, s[68:69]
	global_load_dword v73, v[2:3], off nt
	v_lshl_add_u64 v[2:3], v[2:3], 0, s[68:69]
	global_load_dword v74, v[2:3], off nt
	v_lshl_add_u64 v[2:3], v[2:3], 0, s[68:69]
	global_load_dword v75, v[2:3], off nt
	v_lshl_add_u64 v[2:3], v[2:3], 0, s[68:69]
	global_load_dword v76, v[2:3], off nt
	v_lshl_add_u64 v[2:3], v[2:3], 0, s[68:69]
	global_load_dword v77, v[2:3], off nt
	v_lshl_add_u64 v[2:3], v[2:3], 0, s[68:69]
	global_load_dword v78, v[2:3], off nt
	v_lshl_add_u64 v[2:3], v[2:3], 0, s[68:69]
	global_load_dword v79, v[2:3], off nt
	v_lshl_add_u64 v[2:3], v[2:3], 0, s[68:69]
	global_load_dword v80, v[2:3], off nt
	v_lshl_add_u64 v[2:3], v[2:3], 0, s[68:69]
	global_load_dword v81, v[2:3], off nt
	v_lshl_add_u64 v[2:3], v[2:3], 0, s[68:69]
	global_load_dword v82, v[2:3], off nt

; #define GAS __attribute__((address_space(1)))
; DI void w_load(const WItem& w, int lane, float (&v)[32]) {
;     const int cc = lane & 31, ccl = cc < w.nv ? cc : 0; const GAS float* wp = (const GAS float*)w.W + (size_t)(64 * w.kb + (lane >> 5)) * w.N + w.c0 + ccl;
; #pragma unroll
;     for (int i = 0; i < 32; ++i) v[i] = wp[(size_t)(2 * i) * w.N];
; }
.LBB0_1526:
	s_waitcnt vmcnt(31)
	v_lshl_or_b32 v6, s80, 6, v40
	v_cmp_gt_u32_e32 vcc, s78, v1
	s_waitcnt vmcnt(30)
	v_mul_hi_u32_u24_e32 v7, s66, v6
	v_mul_u32_u24_e32 v6, s66, v6
	s_waitcnt vmcnt(29)
	v_cndmask_b32_e32 v8, 0, v1, vcc
	v_lshl_add_u64 v[6:7], v[6:7], 2, s[62:63]
	s_ashr_i32 s61, s60, 31
	v_lshl_add_u64 v[6:7], s[60:61], 2, v[6:7]
	v_lshlrev_b32_e32 v8, 2, v8
	s_waitcnt vmcnt(28)
	v_mov_b32_e32 v9, v4
	v_lshl_add_u64 v[8:9], v[6:7], 0, v[8:9]
	s_lshl_b32 s68, s66, 3
	global_load_dword v6, v[8:9], off nt
	v_lshl_add_u64 v[8:9], v[8:9], 0, s[68:69]
	s_waitcnt vmcnt(27)
	v_lshl_add_u64 v[10:11], v[8:9], 0, s[68:69]
	global_load_dword v7, v[8:9], off nt
	s_mov_b32 s81, s80
	global_load_dword v8, v[10:11], off nt
	v_lshl_add_u64 v[10:11], v[10:11], 0, s[68:69]
	s_waitcnt vmcnt(27)
	v_lshl_add_u64 v[12:13], v[10:11], 0, s[68:69]
	global_load_dword v9, v[10:11], off nt
	s_nop 0
	global_load_dword v10, v[12:13], off nt
	v_lshl_add_u64 v[12:13], v[12:13], 0, s[68:69]
	s_waitcnt vmcnt(27)
	v_lshl_add_u64 v[14:15], v[12:13], 0, s[68:69]
	global_load_dword v11, v[12:13], off nt
	s_nop 0
	global_load_dword v12, v[14:15], off nt
	v_lshl_add_u64 v[14:15], v[14:15], 0, s[68:69]
	s_waitcnt vmcnt(27)
	v_lshl_add_u64 v[16:17], v[14:15], 0, s[68:69]
	global_load_dword v13, v[14:15], off nt
	s_nop 0
	global_load_dword v14, v[16:17], off nt
	v_lshl_add_u64 v[16:17], v[16:17], 0, s[68:69]
	s_waitcnt vmcnt(27)
	v_lshl_add_u64 v[18:19], v[16:17], 0, s[68:69]
	global_load_dword v15, v[16:17], off nt
	s_nop 0
	global_load_dword v16, v[18:19], off nt
	v_lshl_add_u64 v[18:19], v[18:19], 0, s[68:69]
	s_waitcnt vmcnt(27)
	v_lshl_add_u64 v[20:21], v[18:19], 0, s[68:69]
	global_load_dword v17, v[18:19], off nt
	s_nop 0
	global_load_dword v18, v[20:21], off nt
	v_lshl_add_u64 v[20:21], v[20:21], 0, s[68:69]
	s_waitcnt vmcnt(27)
	v_lshl_add_u64 v[22:23], v[20:21], 0, s[68:69]
	global_load_dword v19, v[20:21], off nt
	s_nop 0
	global_load_dword v20, v[22:23], off nt
	v_lshl_add_u64 v[22:23], v[22:23], 0, s[68:69]
	s_waitcnt vmcnt(27)
	v_lshl_add_u64 v[24:25], v[22:23], 0, s[68:69]
	global_load_dword v21, v[22:23], off nt
	s_nop 0
	global_load_dword v22, v[24:25], off nt
	v_lshl_add_u64 v[24:25], v[24:25], 0, s[68:69]
	s_waitcnt vmcnt(27)
	v_lshl_add_u64 v[26:27], v[24:25], 0, s[68:69]
	global_load_dword v23, v[24:25], off nt
	s_nop 0
	global_load_dword v24, v[26:27], off nt
	v_lshl_add_u64 v[26:27], v[26:27], 0, s[68:69]
	s_waitcnt vmcnt(27)
	v_lshl_add_u64 v[28:29], v[26:27], 0, s[68:69]
	global_load_dword v25, v[26:27], off nt
	s_nop 0
	global_load_dword v26, v[28:29], off nt
	v_lshl_add_u64 v[28:29], v[28:29], 0, s[68:69]
	s_waitcnt vmcnt(27)
	v_lshl_add_u64 v[30:31], v[28:29], 0, s[68:69]
	global_load_dword v27, v[28:29], off nt
	s_nop 0
	global_load_dword v28, v[30:31], off nt
	v_lshl_add_u64 v[30:31], v[30:31], 0, s[68:69]
	s_waitcnt vmcnt(27)
	v_lshl_add_u64 v[32:33], v[30:31], 0, s[68:69]
	global_load_dword v29, v[30:31], off nt
	s_nop 0
	global_load_dword v30, v[32:33], off nt
	v_lshl_add_u64 v[32:33], v[32:33], 0, s[68:69]
	s_waitcnt vmcnt(27)
	v_lshl_add_u64 v[34:35], v[32:33], 0, s[68:69]
	global_load_dword v31, v[32:33], off nt
	s_nop 0
	global_load_dword v32, v[34:35], off nt
	v_lshl_add_u64 v[34:35], v[34:35], 0, s[68:69]
	s_waitcnt vmcnt(27)
	v_lshl_add_u64 v[36:37], v[34:35], 0, s[68:69]
	global_load_dword v33, v[34:35], off nt
	s_nop 0
	global_load_dword v34, v[36:37], off nt
	v_lshl_add_u64 v[36:37], v[36:37], 0, s[68:69]
	v_lshl_add_u64 v[84:85], v[36:37], 0, s[68:69]
	global_load_dword v35, v[36:37], off nt
	s_nop 0
	global_load_dword v36, v[84:85], off nt
	v_lshl_add_u64 v[84:85], v[84:85], 0, s[68:69]
	global_load_dword v37, v[84:85], off nt
	s_andn2_b64 vcc, exec, s[56:57]
	s_cbranch_vccz .LBB0_1479

; #define GAS __attribute__((address_space(1)))
; DI void w_load(const WItem& w, int lane, float (&v)[32]) {
;     const int cc = lane & 31, ccl = cc < w.nv ? cc : 0; const GAS float* wp = (const GAS float*)w.W + (size_t)(64 * w.kb + (lane >> 5)) * w.N + w.c0 + ccl;
; #pragma unroll
;     for (int i = 0; i < 32; ++i) v[i] = wp[(size_t)(2 * i) * w.N];
; }
.LBB0_1571:
	v_lshl_or_b32 v40, s83, 6, v40
	v_cmp_gt_u32_e32 vcc, s84, v1
	s_waitcnt vmcnt(29)
	v_mul_hi_u32_u24_e32 v53, s40, v40
	v_mul_u32_u24_e32 v52, s40, v40
	v_cndmask_b32_e32 v51, 0, v1, vcc
	v_lshl_add_u64 v[52:53], v[52:53], 2, s[30:31]
	s_ashr_i32 s55, s54, 31
	v_lshl_add_u64 v[52:53], s[54:55], 2, v[52:53]
	s_waitcnt vmcnt(28)
	v_lshlrev_b32_e32 v54, 2, v51
	s_waitcnt vmcnt(27)
	v_mov_b32_e32 v55, v4
	v_lshl_add_u64 v[52:53], v[52:53], 0, v[54:55]
	s_lshl_b32 s68, s40, 3
	v_lshl_add_u64 v[54:55], v[52:53], 0, s[68:69]
	global_load_dword v51, v[52:53], off nt
	s_mov_b64 s[54:55], s[16:17]
	global_load_dword v52, v[54:55], off nt
	v_lshl_add_u64 v[54:55], v[54:55], 0, s[68:69]
	s_waitcnt vmcnt(27)
	v_lshl_add_u64 v[56:57], v[54:55], 0, s[68:69]
	global_load_dword v53, v[54:55], off nt
	s_nop 0
	global_load_dword v54, v[56:57], off nt
	v_lshl_add_u64 v[56:57], v[56:57], 0, s[68:69]
	s_waitcnt vmcnt(27)
	v_lshl_add_u64 v[58:59], v[56:57], 0, s[68:69]
	global_load_dword v55, v[56:57], off nt
	s_nop 0
	global_load_dword v56, v[58:59], off nt
	v_lshl_add_u64 v[58:59], v[58:59], 0, s[68:69]
	s_waitcnt vmcnt(27)
	v_lshl_add_u64 v[60:61], v[58:59], 0, s[68:69]
	global_load_dword v57, v[58:59], off nt
	s_nop 0
	global_load_dword v58, v[60:61], off nt
	v_lshl_add_u64 v[60:61], v[60:61], 0, s[68:69]
	s_waitcnt vmcnt(27)
	v_lshl_add_u64 v[62:63], v[60:61], 0, s[68:69]
	global_load_dword v59, v[60:61], off nt
	s_nop 0
	global_load_dword v60, v[62:63], off nt
	v_lshl_add_u64 v[62:63], v[62:63], 0, s[68:69]
	s_waitcnt vmcnt(27)
	v_lshl_add_u64 v[64:65], v[62:63], 0, s[68:69]
	global_load_dword v61, v[62:63], off nt
	s_nop 0
	global_load_dword v62, v[64:65], off nt
	v_lshl_add_u64 v[64:65], v[64:65], 0, s[68:69]
	s_waitcnt vmcnt(27)
	v_lshl_add_u64 v[66:67], v[64:65], 0, s[68:69]
	global_load_dword v63, v[64:65], off nt
	s_nop 0
	global_load_dword v64, v[66:67], off nt
	v_lshl_add_u64 v[66:67], v[66:67], 0, s[68:69]
	s_waitcnt vmcnt(27)
	v_lshl_add_u64 v[68:69], v[66:67], 0, s[68:69]
	global_load_dword v65, v[66:67], off nt
	s_nop 0
	global_load_dword v66, v[68:69], off nt
	v_lshl_add_u64 v[68:69], v[68:69], 0, s[68:69]
	s_waitcnt vmcnt(27)
	v_lshl_add_u64 v[70:71], v[68:69], 0, s[68:69]
	global_load_dword v67, v[68:69], off nt
	s_nop 0
	global_load_dword v68, v[70:71], off nt
	v_lshl_add_u64 v[70:71], v[70:71], 0, s[68:69]
	s_waitcnt vmcnt(27)
	v_lshl_add_u64 v[72:73], v[70:71], 0, s[68:69]
	global_load_dword v69, v[70:71], off nt
	s_nop 0
	global_load_dword v70, v[72:73], off nt
	v_lshl_add_u64 v[72:73], v[72:73], 0, s[68:69]
	s_waitcnt vmcnt(27)
	v_lshl_add_u64 v[74:75], v[72:73], 0, s[68:69]
	global_load_dword v71, v[72:73], off nt
	s_nop 0
	global_load_dword v72, v[74:75], off nt
	v_lshl_add_u64 v[74:75], v[74:75], 0, s[68:69]
	s_waitcnt vmcnt(27)
	v_lshl_add_u64 v[76:77], v[74:75], 0, s[68:69]
	global_load_dword v73, v[74:75], off nt
	s_nop 0
	global_load_dword v74, v[76:77], off nt
	v_lshl_add_u64 v[76:77], v[76:77], 0, s[68:69]
	s_waitcnt vmcnt(27)
	v_lshl_add_u64 v[78:79], v[76:77], 0, s[68:69]
	global_load_dword v75, v[76:77], off nt
	s_nop 0
	global_load_dword v76, v[78:79], off nt
	v_lshl_add_u64 v[78:79], v[78:79], 0, s[68:69]
	s_waitcnt vmcnt(27)
	v_lshl_add_u64 v[80:81], v[78:79], 0, s[68:69]
	global_load_dword v77, v[78:79], off nt
	s_nop 0
	global_load_dword v78, v[80:81], off nt
	v_lshl_add_u64 v[80:81], v[80:81], 0, s[68:69]
	s_waitcnt vmcnt(28)
	v_lshl_add_u64 v[82:83], v[80:81], 0, s[68:69]
	global_load_dword v79, v[80:81], off nt
	s_nop 0
	global_load_dword v80, v[82:83], off nt
	v_lshl_add_u64 v[82:83], v[82:83], 0, s[68:69]
	global_load_dword v81, v[82:83], off nt
	v_lshl_add_u64 v[82:83], v[82:83], 0, s[68:69]
	global_load_dword v82, v[82:83], off nt
	s_andn2_b64 vcc, exec, s[58:59]
	s_cbranch_vccz .LBB0_1481

; #define GAS __attribute__((address_space(1)))
; DI void w_load(const WItem& w, int lane, float (&v)[32]) {
;     const int cc = lane & 31, ccl = cc < w.nv ? cc : 0; const GAS float* wp = (const GAS float*)w.W + (size_t)(64 * w.kb + (lane >> 5)) * w.N + w.c0 + ccl;
; #pragma unroll
;     for (int i = 0; i < 32; ++i) v[i] = wp[(size_t)(2 * i) * w.N];
; }
.LBB0_1716:
	v_lshl_or_b32 v2, s81, 6, v40
	v_cmp_gt_u32_e32 vcc, s78, v1
	v_mul_hi_u32_u24_e32 v3, s58, v2
	v_mul_u32_u24_e32 v2, s58, v2
	v_cndmask_b32_e32 v5, 0, v1, vcc
	v_lshl_add_u64 v[2:3], v[2:3], 2, s[30:31]
	s_ashr_i32 s1, s0, 31
	v_lshl_add_u64 v[2:3], s[0:1], 2, v[2:3]
	v_lshlrev_b32_e32 v6, 2, v5
	v_mov_b32_e32 v7, v4
	v_lshl_add_u64 v[2:3], v[2:3], 0, v[6:7]
	s_lshl_b32 s68, s58, 3
	global_load_dword v6, v[2:3], off nt
	v_lshl_add_u64 v[2:3], v[2:3], 0, s[68:69]
	global_load_dword v7, v[2:3], off nt
	v_lshl_add_u64 v[2:3], v[2:3], 0, s[68:69]
	global_load_dword v8, v[2:3], off nt
	v_lshl_add_u64 v[2:3], v[2:3], 0, s[68:69]
	global_load_dword v9, v[2:3], off nt
	v_lshl_add_u64 v[2:3], v[2:3], 0, s[68:69]
	global_load_dword v10, v[2:3], off nt
	v_lshl_add_u64 v[2:3], v[2:3], 0, s[68:69]
	global_load_dword v11, v[2:3], off nt
	v_lshl_add_u64 v[2:3], v[2:3], 0, s[68:69]
	global_load_dword v12, v[2:3], off nt
	v_lshl_add_u64 v[2:3], v[2:3], 0, s[68:69]
	global_load_dword v13, v[2:3], off nt
	v_lshl_add_u64 v[2:3], v[2:3], 0, s[68:69]
	global_load_dword v14, v[2:3], off nt
	v_lshl_add_u64 v[2:3], v[2:3], 0, s[68:69]
	global_load_dword v15, v[2:3], off nt
	v_lshl_add_u64 v[2:3], v[2:3], 0, s[68:69]
	global_load_dword v16, v[2:3], off nt
	v_lshl_add_u64 v[2:3], v[2:3], 0, s[68:69]
	global_load_dword v17, v[2:3], off nt
	v_lshl_add_u64 v[2:3], v[2:3], 0, s[68:69]
	global_load_dword v18, v[2:3], off nt
	v_lshl_add_u64 v[2:3], v[2:3], 0, s[68:69]
	global_load_dword v19, v[2:3], off nt
	v_lshl_add_u64 v[2:3], v[2:3], 0, s[68:69]
	global_load_dword v20, v[2:3], off nt
	v_lshl_add_u64 v[2:3], v[2:3], 0, s[68:69]
	global_load_dword v21, v[2:3], off nt
	v_lshl_add_u64 v[2:3], v[2:3], 0, s[68:69]
	global_load_dword v22, v[2:3], off nt
	v_lshl_add_u64 v[2:3], v[2:3], 0, s[68:69]
	global_load_dword v23, v[2:3], off nt
	v_lshl_add_u64 v[2:3], v[2:3], 0, s[68:69]
	global_load_dword v24, v[2:3], off nt
	v_lshl_add_u64 v[2:3], v[2:3], 0, s[68:69]
	global_load_dword v25, v[2:3], off nt
	v_lshl_add_u64 v[2:3], v[2:3], 0, s[68:69]
	global_load_dword v26, v[2:3], off nt
	v_lshl_add_u64 v[2:3], v[2:3], 0, s[68:69]
	global_load_dword v27, v[2:3], off nt
	v_lshl_add_u64 v[2:3], v[2:3], 0, s[68:69]
	global_load_dword v28, v[2:3], off nt
	v_lshl_add_u64 v[2:3], v[2:3], 0, s[68:69]
	global_load_dword v29, v[2:3], off nt
	v_lshl_add_u64 v[2:3], v[2:3], 0, s[68:69]
	global_load_dword v30, v[2:3], off nt
	v_lshl_add_u64 v[2:3], v[2:3], 0, s[68:69]
	global_load_dword v31, v[2:3], off nt
	v_lshl_add_u64 v[2:3], v[2:3], 0, s[68:69]
	global_load_dword v32, v[2:3], off nt
	v_lshl_add_u64 v[2:3], v[2:3], 0, s[68:69]
	global_load_dword v33, v[2:3], off nt
	v_lshl_add_u64 v[2:3], v[2:3], 0, s[68:69]
	global_load_dword v34, v[2:3], off nt
	v_lshl_add_u64 v[2:3], v[2:3], 0, s[68:69]
	global_load_dword v35, v[2:3], off nt
	v_lshl_add_u64 v[2:3], v[2:3], 0, s[68:69]
	global_load_dword v36, v[2:3], off nt
	v_lshl_add_u64 v[2:3], v[2:3], 0, s[68:69]
	global_load_dword v37, v[2:3], off nt
	s_cmpk_lt_i32 s76, 0x7878
	s_cselect_b64 s[30:31], -1, 0
	s_cmpk_gt_i32 s76, 0x7877
	s_cbranch_scc1 .LBB0_1761

; #define GAS __attribute__((address_space(1)))
; DI void w_load(const WItem& w, int lane, float (&v)[32]) {
;     const int cc = lane & 31, ccl = cc < w.nv ? cc : 0; const GAS float* wp = (const GAS float*)w.W + (size_t)(64 * w.kb + (lane >> 5)) * w.N + w.c0 + ccl;
; #pragma unroll
;     for (int i = 0; i < 32; ++i) v[i] = wp[(size_t)(2 * i) * w.N];
; }
.LBB0_1760:
	v_lshl_or_b32 v2, s83, 6, v40
	v_cmp_gt_u32_e32 vcc, s84, v1
	v_mul_hi_u32_u24_e32 v3, s62, v2
	v_mul_u32_u24_e32 v2, s62, v2
	v_cndmask_b32_e32 v5, 0, v1, vcc
	v_lshl_add_u64 v[2:3], v[2:3], 2, s[60:61]
	s_ashr_i32 s59, s58, 31
	v_lshl_add_u64 v[2:3], s[58:59], 2, v[2:3]
	v_lshlrev_b32_e32 v44, 2, v5
	v_mov_b32_e32 v45, v4
	v_lshl_add_u64 v[2:3], v[2:3], 0, v[44:45]
	s_lshl_b32 s68, s62, 3
	global_load_dword v51, v[2:3], off nt
	v_lshl_add_u64 v[2:3], v[2:3], 0, s[68:69]
	global_load_dword v52, v[2:3], off nt
	v_lshl_add_u64 v[2:3], v[2:3], 0, s[68:69]
	global_load_dword v53, v[2:3], off nt
	v_lshl_add_u64 v[2:3], v[2:3], 0, s[68:69]
	global_load_dword v54, v[2:3], off nt
	v_lshl_add_u64 v[2:3], v[2:3], 0, s[68:69]
	global_load_dword v55, v[2:3], off nt
	v_lshl_add_u64 v[2:3], v[2:3], 0, s[68:69]
	global_load_dword v56, v[2:3], off nt
	v_lshl_add_u64 v[2:3], v[2:3], 0, s[68:69]
	global_load_dword v57, v[2:3], off nt
	v_lshl_add_u64 v[2:3], v[2:3], 0, s[68:69]
	global_load_dword v58, v[2:3], off nt
	v_lshl_add_u64 v[2:3], v[2:3], 0, s[68:69]
	global_load_dword v59, v[2:3], off nt
	v_lshl_add_u64 v[2:3], v[2:3], 0, s[68:69]
	global_load_dword v60, v[2:3], off nt
	v_lshl_add_u64 v[2:3], v[2:3], 0, s[68:69]
	global_load_dword v61, v[2:3], off nt
	v_lshl_add_u64 v[2:3], v[2:3], 0, s[68:69]
	global_load_dword v62, v[2:3], off nt
	v_lshl_add_u64 v[2:3], v[2:3], 0, s[68:69]
	global_load_dword v63, v[2:3], off nt
	v_lshl_add_u64 v[2:3], v[2:3], 0, s[68:69]
	global_load_dword v64, v[2:3], off nt
	v_lshl_add_u64 v[2:3], v[2:3], 0, s[68:69]
	global_load_dword v65, v[2:3], off nt
	v_lshl_add_u64 v[2:3], v[2:3], 0, s[68:69]
	global_load_dword v66, v[2:3], off nt
	v_lshl_add_u64 v[2:3], v[2:3], 0, s[68:69]
	global_load_dword v67, v[2:3], off nt
	v_lshl_add_u64 v[2:3], v[2:3], 0, s[68:69]
	global_load_dword v68, v[2:3], off nt
	v_lshl_add_u64 v[2:3], v[2:3], 0, s[68:69]
	global_load_dword v69, v[2:3], off nt
	v_lshl_add_u64 v[2:3], v[2:3], 0, s[68:69]
	global_load_dword v70, v[2:3], off nt
	v_lshl_add_u64 v[2:3], v[2:3], 0, s[68:69]
	global_load_dword v71, v[2:3], off nt
	v_lshl_add_u64 v[2:3], v[2:3], 0, s[68:69]
	global_load_dword v72, v[2:3], off nt
	v_lshl_add_u64 v[2:3], v[2:3], 0, s[68:69]
	global_load_dword v73, v[2:3], off nt
	v_lshl_add_u64 v[2:3], v[2:3], 0, s[68:69]
	global_load_dword v74, v[2:3], off nt
	v_lshl_add_u64 v[2:3], v[2:3], 0, s[68:69]
	global_load_dword v75, v[2:3], off nt
	v_lshl_add_u64 v[2:3], v[2:3], 0, s[68:69]
	global_load_dword v76, v[2:3], off nt
	v_lshl_add_u64 v[2:3], v[2:3], 0, s[68:69]
	global_load_dword v77, v[2:3], off nt
	v_lshl_add_u64 v[2:3], v[2:3], 0, s[68:69]
	global_load_dword v78, v[2:3], off nt
	v_lshl_add_u64 v[2:3], v[2:3], 0, s[68:69]
	global_load_dword v79, v[2:3], off nt
	v_lshl_add_u64 v[2:3], v[2:3], 0, s[68:69]
	global_load_dword v80, v[2:3], off nt
	v_lshl_add_u64 v[2:3], v[2:3], 0, s[68:69]
	global_load_dword v81, v[2:3], off nt
	v_lshl_add_u64 v[2:3], v[2:3], 0, s[68:69]
	global_load_dword v82, v[2:3], off nt

; #define GAS __attribute__((address_space(1)))
; DI void w_load(const WItem& w, int lane, float (&v)[32]) {
;     const int cc = lane & 31, ccl = cc < w.nv ? cc : 0; const GAS float* wp = (const GAS float*)w.W + (size_t)(64 * w.kb + (lane >> 5)) * w.N + w.c0 + ccl;
; #pragma unroll
;     for (int i = 0; i < 32; ++i) v[i] = wp[(size_t)(2 * i) * w.N];
; }
.LBB0_1811:
	s_waitcnt vmcnt(31)
	v_lshl_or_b32 v6, s80, 6, v40
	v_cmp_gt_u32_e32 vcc, s78, v1
	s_waitcnt vmcnt(30)
	v_mul_hi_u32_u24_e32 v7, s62, v6
	v_mul_u32_u24_e32 v6, s62, v6
	s_waitcnt vmcnt(29)
	v_cndmask_b32_e32 v8, 0, v1, vcc
	v_lshl_add_u64 v[6:7], v[6:7], 2, s[60:61]
	s_ashr_i32 s59, s58, 31
	v_lshl_add_u64 v[6:7], s[58:59], 2, v[6:7]
	v_lshlrev_b32_e32 v8, 2, v8
	s_waitcnt vmcnt(28)
	v_mov_b32_e32 v9, v4
	v_lshl_add_u64 v[8:9], v[6:7], 0, v[8:9]
	s_lshl_b32 s68, s62, 3
	global_load_dword v6, v[8:9], off nt
	v_lshl_add_u64 v[8:9], v[8:9], 0, s[68:69]
	s_waitcnt vmcnt(27)
	v_lshl_add_u64 v[10:11], v[8:9], 0, s[68:69]
	global_load_dword v7, v[8:9], off nt
	s_mov_b32 s81, s80
	global_load_dword v8, v[10:11], off nt
	v_lshl_add_u64 v[10:11], v[10:11], 0, s[68:69]
	s_waitcnt vmcnt(27)
	v_lshl_add_u64 v[12:13], v[10:11], 0, s[68:69]
	global_load_dword v9, v[10:11], off nt
	s_nop 0
	global_load_dword v10, v[12:13], off nt
	v_lshl_add_u64 v[12:13], v[12:13], 0, s[68:69]
	s_waitcnt vmcnt(27)
	v_lshl_add_u64 v[14:15], v[12:13], 0, s[68:69]
	global_load_dword v11, v[12:13], off nt
	s_nop 0
	global_load_dword v12, v[14:15], off nt
	v_lshl_add_u64 v[14:15], v[14:15], 0, s[68:69]
	s_waitcnt vmcnt(27)
	v_lshl_add_u64 v[16:17], v[14:15], 0, s[68:69]
	global_load_dword v13, v[14:15], off nt
	s_nop 0
	global_load_dword v14, v[16:17], off nt
	v_lshl_add_u64 v[16:17], v[16:17], 0, s[68:69]
	s_waitcnt vmcnt(27)
	v_lshl_add_u64 v[18:19], v[16:17], 0, s[68:69]
	global_load_dword v15, v[16:17], off nt
	s_nop 0
	global_load_dword v16, v[18:19], off nt
	v_lshl_add_u64 v[18:19], v[18:19], 0, s[68:69]
	s_waitcnt vmcnt(27)
	v_lshl_add_u64 v[20:21], v[18:19], 0, s[68:69]
	global_load_dword v17, v[18:19], off nt
	s_nop 0
	global_load_dword v18, v[20:21], off nt
	v_lshl_add_u64 v[20:21], v[20:21], 0, s[68:69]
	s_waitcnt vmcnt(27)
	v_lshl_add_u64 v[22:23], v[20:21], 0, s[68:69]
	global_load_dword v19, v[20:21], off nt
	s_nop 0
	global_load_dword v20, v[22:23], off nt
	v_lshl_add_u64 v[22:23], v[22:23], 0, s[68:69]
	s_waitcnt vmcnt(27)
	v_lshl_add_u64 v[24:25], v[22:23], 0, s[68:69]
	global_load_dword v21, v[22:23], off nt
	s_nop 0
	global_load_dword v22, v[24:25], off nt
	v_lshl_add_u64 v[24:25], v[24:25], 0, s[68:69]
	s_waitcnt vmcnt(27)
	v_lshl_add_u64 v[26:27], v[24:25], 0, s[68:69]
	global_load_dword v23, v[24:25], off nt
	s_nop 0
	global_load_dword v24, v[26:27], off nt
	v_lshl_add_u64 v[26:27], v[26:27], 0, s[68:69]
	s_waitcnt vmcnt(27)
	v_lshl_add_u64 v[28:29], v[26:27], 0, s[68:69]
	global_load_dword v25, v[26:27], off nt
	s_nop 0
	global_load_dword v26, v[28:29], off nt
	v_lshl_add_u64 v[28:29], v[28:29], 0, s[68:69]
	s_waitcnt vmcnt(27)
	v_lshl_add_u64 v[30:31], v[28:29], 0, s[68:69]
	global_load_dword v27, v[28:29], off nt
	s_nop 0
	global_load_dword v28, v[30:31], off nt
	v_lshl_add_u64 v[30:31], v[30:31], 0, s[68:69]
	s_waitcnt vmcnt(27)
	v_lshl_add_u64 v[32:33], v[30:31], 0, s[68:69]
	global_load_dword v29, v[30:31], off nt
	s_nop 0
	global_load_dword v30, v[32:33], off nt
	v_lshl_add_u64 v[32:33], v[32:33], 0, s[68:69]
	s_waitcnt vmcnt(27)
	v_lshl_add_u64 v[34:35], v[32:33], 0, s[68:69]
	global_load_dword v31, v[32:33], off nt
	s_nop 0
	global_load_dword v32, v[34:35], off nt
	v_lshl_add_u64 v[34:35], v[34:35], 0, s[68:69]
	s_waitcnt vmcnt(27)
	v_lshl_add_u64 v[36:37], v[34:35], 0, s[68:69]
	global_load_dword v33, v[34:35], off nt
	s_nop 0
	global_load_dword v34, v[36:37], off nt
	v_lshl_add_u64 v[36:37], v[36:37], 0, s[68:69]
	v_lshl_add_u64 v[84:85], v[36:37], 0, s[68:69]
	global_load_dword v35, v[36:37], off nt
	s_nop 0
	global_load_dword v36, v[84:85], off nt
	v_lshl_add_u64 v[84:85], v[84:85], 0, s[68:69]
	global_load_dword v37, v[84:85], off nt
	s_andn2_b64 vcc, exec, s[30:31]
	s_cbranch_vccz .LBB0_1764

; #define GAS __attribute__((address_space(1)))
; DI void w_load(const WItem& w, int lane, float (&v)[32]) {
;     const int cc = lane & 31, ccl = cc < w.nv ? cc : 0; const GAS float* wp = (const GAS float*)w.W + (size_t)(64 * w.kb + (lane >> 5)) * w.N + w.c0 + ccl;
; #pragma unroll
;     for (int i = 0; i < 32; ++i) v[i] = wp[(size_t)(2 * i) * w.N];
; }
.LBB0_1856:
	v_lshl_or_b32 v40, s83, 6, v40
	v_cmp_gt_u32_e32 vcc, s84, v1
	s_waitcnt vmcnt(29)
	v_mul_hi_u32_u24_e32 v53, s42, v40
	v_mul_u32_u24_e32 v52, s42, v40
	v_cndmask_b32_e32 v51, 0, v1, vcc
	v_lshl_add_u64 v[52:53], v[52:53], 2, s[40:41]
	s_ashr_i32 s1, s0, 31
	v_lshl_add_u64 v[52:53], s[0:1], 2, v[52:53]
	s_waitcnt vmcnt(28)
	v_lshlrev_b32_e32 v54, 2, v51
	s_waitcnt vmcnt(27)
	v_mov_b32_e32 v55, v4
	v_lshl_add_u64 v[52:53], v[52:53], 0, v[54:55]
	s_lshl_b32 s68, s42, 3
	v_lshl_add_u64 v[54:55], v[52:53], 0, s[68:69]
	global_load_dword v51, v[52:53], off nt
	s_mov_b64 s[0:1], s[16:17]
	global_load_dword v52, v[54:55], off nt
	v_lshl_add_u64 v[54:55], v[54:55], 0, s[68:69]
	s_waitcnt vmcnt(27)
	v_lshl_add_u64 v[56:57], v[54:55], 0, s[68:69]
	global_load_dword v53, v[54:55], off nt
	s_nop 0
	global_load_dword v54, v[56:57], off nt
	v_lshl_add_u64 v[56:57], v[56:57], 0, s[68:69]
	s_waitcnt vmcnt(27)
	v_lshl_add_u64 v[58:59], v[56:57], 0, s[68:69]
	global_load_dword v55, v[56:57], off nt
	s_nop 0
	global_load_dword v56, v[58:59], off nt
	v_lshl_add_u64 v[58:59], v[58:59], 0, s[68:69]
	s_waitcnt vmcnt(27)
	v_lshl_add_u64 v[60:61], v[58:59], 0, s[68:69]
	global_load_dword v57, v[58:59], off nt
	s_nop 0
	global_load_dword v58, v[60:61], off nt
	v_lshl_add_u64 v[60:61], v[60:61], 0, s[68:69]
	s_waitcnt vmcnt(27)
	v_lshl_add_u64 v[62:63], v[60:61], 0, s[68:69]
	global_load_dword v59, v[60:61], off nt
	s_nop 0
	global_load_dword v60, v[62:63], off nt
	v_lshl_add_u64 v[62:63], v[62:63], 0, s[68:69]
	s_waitcnt vmcnt(27)
	v_lshl_add_u64 v[64:65], v[62:63], 0, s[68:69]
	global_load_dword v61, v[62:63], off nt
	s_nop 0
	global_load_dword v62, v[64:65], off nt
	v_lshl_add_u64 v[64:65], v[64:65], 0, s[68:69]
	s_waitcnt vmcnt(27)
	v_lshl_add_u64 v[66:67], v[64:65], 0, s[68:69]
	global_load_dword v63, v[64:65], off nt
	s_nop 0
	global_load_dword v64, v[66:67], off nt
	v_lshl_add_u64 v[66:67], v[66:67], 0, s[68:69]
	s_waitcnt vmcnt(27)
	v_lshl_add_u64 v[68:69], v[66:67], 0, s[68:69]
	global_load_dword v65, v[66:67], off nt
	s_nop 0
	global_load_dword v66, v[68:69], off nt
	v_lshl_add_u64 v[68:69], v[68:69], 0, s[68:69]
	s_waitcnt vmcnt(27)
	v_lshl_add_u64 v[70:71], v[68:69], 0, s[68:69]
	global_load_dword v67, v[68:69], off nt
	s_nop 0
	global_load_dword v68, v[70:71], off nt
	v_lshl_add_u64 v[70:71], v[70:71], 0, s[68:69]
	s_waitcnt vmcnt(27)
	v_lshl_add_u64 v[72:73], v[70:71], 0, s[68:69]
	global_load_dword v69, v[70:71], off nt
	s_nop 0
	global_load_dword v70, v[72:73], off nt
	v_lshl_add_u64 v[72:73], v[72:73], 0, s[68:69]
	s_waitcnt vmcnt(27)
	v_lshl_add_u64 v[74:75], v[72:73], 0, s[68:69]
	global_load_dword v71, v[72:73], off nt
	s_nop 0
	global_load_dword v72, v[74:75], off nt
	v_lshl_add_u64 v[74:75], v[74:75], 0, s[68:69]
	s_waitcnt vmcnt(27)
	v_lshl_add_u64 v[76:77], v[74:75], 0, s[68:69]
	global_load_dword v73, v[74:75], off nt
	s_nop 0
	global_load_dword v74, v[76:77], off nt
	v_lshl_add_u64 v[76:77], v[76:77], 0, s[68:69]
	s_waitcnt vmcnt(27)
	v_lshl_add_u64 v[78:79], v[76:77], 0, s[68:69]
	global_load_dword v75, v[76:77], off nt
	s_nop 0
	global_load_dword v76, v[78:79], off nt
	v_lshl_add_u64 v[78:79], v[78:79], 0, s[68:69]
	s_waitcnt vmcnt(27)
	v_lshl_add_u64 v[80:81], v[78:79], 0, s[68:69]
	global_load_dword v77, v[78:79], off nt
	s_nop 0
	global_load_dword v78, v[80:81], off nt
	v_lshl_add_u64 v[80:81], v[80:81], 0, s[68:69]
	s_waitcnt vmcnt(28)
	v_lshl_add_u64 v[82:83], v[80:81], 0, s[68:69]
	global_load_dword v79, v[80:81], off nt
	s_nop 0
	global_load_dword v80, v[82:83], off nt
	v_lshl_add_u64 v[82:83], v[82:83], 0, s[68:69]
	global_load_dword v81, v[82:83], off nt
	v_lshl_add_u64 v[82:83], v[82:83], 0, s[68:69]
	global_load_dword v82, v[82:83], off nt
	s_andn2_b64 vcc, exec, s[56:57]
	s_cbranch_vccz .LBB0_1766
